# split grid barrier 4 for the 16 meta-row projection blocks: arrive at seam, skinny compute before the wait, wave-0 wait before first H1 store
# speedup vs baseline: 1.0199x; 1.0024x over previous
.Lgb_chk_4:
	v_mov_b32_e32 v11, s89
	v_cmp_lt_u32_e32 vcc, 15, v11
	s_cbranch_vccz .Lgb_done_4

.LBB0_817:
	v_add_u32_e32 v12, s6, v222
	v_ashrrev_i32_e32 v13, 31, v12
	v_lshlrev_b64 v[12:13], 11, v[12:13]
	v_lshl_add_u64 v[56:57], v[4:5], 0, v[12:13]
	v_add_co_u32_e32 v58, vcc, 0x8000, v56
	global_load_dwordx4 v[12:15], v[56:57], off
	global_load_dwordx4 v[16:19], v[2:3], off
	v_addc_co_u32_e32 v59, vcc, 0, v57, vcc
	v_add_co_u32_e32 v60, vcc, 0x10000, v56
	global_load_dwordx4 v[20:23], v[58:59], off
	s_nop 0
	v_addc_co_u32_e32 v61, vcc, 0, v57, vcc
	v_add_co_u32_e32 v62, vcc, 0x18000, v56
	global_load_dwordx4 v[24:27], v[60:61], off
	s_nop 0
	v_addc_co_u32_e32 v63, vcc, 0, v57, vcc
	global_load_dwordx4 v[28:31], v[62:63], off
	global_load_dwordx4 v[32:35], v[56:57], off offset:64
	global_load_dwordx4 v[36:39], v[2:3], off offset:64
	global_load_dwordx4 v[40:43], v[58:59], off offset:64
	global_load_dwordx4 v[44:47], v[60:61], off offset:64
	global_load_dwordx4 v[48:51], v[62:63], off offset:64
	s_and_b64 vcc, exec, s[4:5]
	s_waitcnt vmcnt(8)
	v_mfma_f32_16x16x32_bf16 v[12:15], v[12:15], v[16:19], 0
	s_waitcnt vmcnt(7)
	v_mfma_f32_16x16x32_bf16 v[20:23], v[20:23], v[16:19], 0
	s_waitcnt vmcnt(6)
	v_mfma_f32_16x16x32_bf16 v[24:27], v[24:27], v[16:19], 0
	s_waitcnt vmcnt(5)
	v_mfma_f32_16x16x32_bf16 v[16:19], v[28:31], v[16:19], 0
	global_load_dwordx4 v[28:31], v[56:57], off offset:128
	global_load_dwordx4 v[52:55], v[2:3], off offset:128
	s_waitcnt vmcnt(5)
	v_mfma_f32_16x16x32_bf16 v[12:15], v[32:35], v[36:39], v[12:15]
	global_load_dwordx4 v[32:35], v[58:59], off offset:128
	s_waitcnt vmcnt(5)
	v_mfma_f32_16x16x32_bf16 v[20:23], v[40:43], v[36:39], v[20:23]
	global_load_dwordx4 v[40:43], v[60:61], off offset:128
	s_waitcnt vmcnt(5)
	v_mfma_f32_16x16x32_bf16 v[24:27], v[44:47], v[36:39], v[24:27]
	global_load_dwordx4 v[44:47], v[62:63], off offset:128
	s_waitcnt vmcnt(5)
	v_mfma_f32_16x16x32_bf16 v[16:19], v[48:51], v[36:39], v[16:19]
	global_load_dwordx4 v[36:39], v[56:57], off offset:192
	global_load_dwordx4 v[48:51], v[2:3], off offset:192
	s_waitcnt vmcnt(5)
	v_mfma_f32_16x16x32_bf16 v[12:15], v[28:31], v[52:55], v[12:15]
	global_load_dwordx4 v[28:31], v[58:59], off offset:192
	s_waitcnt vmcnt(5)
	v_mfma_f32_16x16x32_bf16 v[20:23], v[32:35], v[52:55], v[20:23]
	global_load_dwordx4 v[32:35], v[60:61], off offset:192
	s_waitcnt vmcnt(5)
	v_mfma_f32_16x16x32_bf16 v[24:27], v[40:43], v[52:55], v[24:27]
	global_load_dwordx4 v[40:43], v[62:63], off offset:192
	s_barrier
	s_waitcnt vmcnt(5)
	v_mfma_f32_16x16x32_bf16 v[16:19], v[44:47], v[52:55], v[16:19]
	s_waitcnt vmcnt(3)
	v_mfma_f32_16x16x32_bf16 v[12:15], v[36:39], v[48:51], v[12:15]
	s_waitcnt vmcnt(2)
	v_mfma_f32_16x16x32_bf16 v[20:23], v[28:31], v[48:51], v[20:23]
	s_waitcnt vmcnt(1)
	v_mfma_f32_16x16x32_bf16 v[24:27], v[32:35], v[48:51], v[24:27]
	s_waitcnt vmcnt(0)
	v_mfma_f32_16x16x32_bf16 v[16:19], v[40:43], v[48:51], v[16:19]
	s_nop 1
	ds_write_b128 v11, v[12:15]
	s_nop 0
	ds_write_b128 v11, v[20:23] offset:1024
	s_nop 0
	ds_write_b128 v11, v[24:27] offset:2048
	s_nop 0
	ds_write_b128 v11, v[16:19] offset:3072
	s_waitcnt lgkmcnt(0)
	s_barrier
	s_cbranch_vccnz .LBB0_816
	v_add_u32_e32 v80, s6, v10
	v_ashrrev_i32_e32 v81, 31, v80
	v_lshl_add_u64 v[82:83], v[80:81], 2, v[6:7]
	global_load_dwordx4 v[12:15], v[82:83], off
	global_load_dwordx4 v[88:91], v[82:83], off offset:64
	global_load_dwordx4 v[92:95], v[82:83], off offset:128
	global_load_dwordx4 v[96:99], v[82:83], off offset:192
	ds_read_b128 v[16:19], v1
	ds_read_b128 v[20:23], v1 offset:1024
	ds_read_b128 v[24:27], v1 offset:4096
	ds_read_b128 v[28:31], v1 offset:5120
	ds_read_b128 v[32:35], v1 offset:8192
	ds_read_b128 v[36:39], v1 offset:9216
	ds_read_b128 v[40:43], v1 offset:12288
	ds_read_b128 v[44:47], v1 offset:13312
	ds_read_b128 v[48:51], v1 offset:16384
	ds_read_b128 v[52:55], v1 offset:17408
	ds_read_b128 v[56:59], v1 offset:20480
	ds_read_b128 v[60:63], v1 offset:21504
	ds_read_b128 v[64:67], v1 offset:24576
	ds_read_b128 v[68:71], v1 offset:25600
	ds_read_b128 v[72:75], v1 offset:28672
	ds_read_b128 v[76:79], v1 offset:29696
	s_waitcnt lgkmcnt(13)
	v_pk_add_f32 v[18:19], v[18:19], v[26:27]
	v_pk_add_f32 v[16:17], v[16:17], v[24:25]
	s_waitcnt lgkmcnt(11)
	v_pk_add_f32 v[18:19], v[18:19], v[34:35]
	v_pk_add_f32 v[16:17], v[16:17], v[32:33]
	s_waitcnt lgkmcnt(9)
	v_pk_add_f32 v[18:19], v[18:19], v[42:43]
	v_pk_add_f32 v[16:17], v[16:17], v[40:41]
	s_waitcnt lgkmcnt(7)
	v_pk_add_f32 v[18:19], v[18:19], v[50:51]
	v_pk_add_f32 v[16:17], v[16:17], v[48:49]
	s_waitcnt lgkmcnt(5)
	v_pk_add_f32 v[18:19], v[18:19], v[58:59]
	v_pk_add_f32 v[16:17], v[16:17], v[56:57]
	s_waitcnt lgkmcnt(3)
	v_pk_add_f32 v[18:19], v[18:19], v[66:67]
	v_pk_add_f32 v[16:17], v[16:17], v[64:65]
	s_waitcnt lgkmcnt(1)
	v_pk_add_f32 v[18:19], v[18:19], v[74:75]
	v_pk_add_f32 v[16:17], v[16:17], v[72:73]
	v_lshl_add_u64 v[84:85], v[80:81], 1, v[8:9]
	v_pk_add_f32 v[20:21], v[20:21], v[28:29]
	s_waitcnt vmcnt(3)
	v_pk_add_f32 v[14:15], v[18:19], v[14:15]
	v_pk_add_f32 v[12:13], v[16:17], v[12:13]
	v_bfe_u32 v18, v14, 16, 1
	v_bfe_u32 v16, v12, 16, 1
	v_bfe_u32 v17, v13, 16, 1
	v_bfe_u32 v19, v15, 16, 1
	v_add3_u32 v12, v12, v16, s8
	v_add3_u32 v14, v14, v18, s8
	v_add3_u32 v13, v13, v17, s8
	v_add3_u32 v15, v15, v19, s8
	v_lshrrev_b32_e32 v12, 16, v12
	v_lshrrev_b32_e32 v14, 16, v14
	v_and_or_b32 v12, v13, s9, v12
	v_and_or_b32 v13, v15, s9, v14
	v_mov_b32_e32 v24, 0x22160
	ds_read_b32 v25, v24
	v_mov_b32_e32 v26, s99
	v_lshrrev_b32_e32 v27, 16, v26
	v_mov_b32_e32 v32, s98
	v_min_u32_e32 v32, 8, v32
	v_mov_b32_e32 v33, 0
	s_waitcnt lgkmcnt(0)
	v_mul_lo_u32 v32, v32, v25
.Lgw_poll_4:
	global_load_dword v34, v27, s[100:101] sc1
	v_add_u32_e32 v33, 1, v33
	s_waitcnt vmcnt(0)
	v_cmp_ge_u32_e32 vcc, v34, v32
	s_cbranch_vccnz .Lgw_end_4
	v_cmp_gt_u32_e32 vcc, 0x80000, v33
	s_sleep 1
	s_cbranch_vccnz .Lgw_poll_4
.Lgw_end_4:
	global_store_dwordx2 v[84:85], v[12:13], off sc1
	v_pk_add_f32 v[18:19], v[22:23], v[30:31]
	v_pk_add_f32 v[20:21], v[20:21], v[36:37]
	v_pk_add_f32 v[18:19], v[18:19], v[38:39]
	v_pk_add_f32 v[20:21], v[20:21], v[44:45]
	v_pk_add_f32 v[18:19], v[18:19], v[46:47]
	v_pk_add_f32 v[20:21], v[20:21], v[52:53]
	v_pk_add_f32 v[18:19], v[18:19], v[54:55]
	v_pk_add_f32 v[20:21], v[20:21], v[60:61]
	v_pk_add_f32 v[18:19], v[18:19], v[62:63]
	v_pk_add_f32 v[20:21], v[20:21], v[68:69]
	v_pk_add_f32 v[18:19], v[18:19], v[70:71]
	s_waitcnt lgkmcnt(0)
	v_pk_add_f32 v[20:21], v[20:21], v[76:77]
	v_pk_add_f32 v[18:19], v[18:19], v[78:79]
	v_add_u32_e32 v16, 16, v80
	v_ashrrev_i32_e32 v17, 31, v16
	v_lshl_add_u64 v[16:17], v[16:17], 1, v[8:9]
	v_add_u32_e32 v84, 32, v80
	v_ashrrev_i32_e32 v85, 31, v84
	v_lshl_add_u64 v[84:85], v[84:85], 1, v[8:9]
	s_waitcnt vmcnt(3)
	v_pk_add_f32 v[14:15], v[18:19], v[90:91]
	v_pk_add_f32 v[12:13], v[20:21], v[88:89]
	v_bfe_u32 v20, v14, 16, 1
	v_bfe_u32 v18, v12, 16, 1
	v_bfe_u32 v19, v13, 16, 1
	v_bfe_u32 v21, v15, 16, 1
	v_add3_u32 v12, v12, v18, s8
	v_add3_u32 v14, v14, v20, s8
	v_add3_u32 v13, v13, v19, s8
	v_add3_u32 v15, v15, v21, s8
	v_lshrrev_b32_e32 v12, 16, v12
	v_lshrrev_b32_e32 v14, 16, v14
	v_and_or_b32 v12, v13, s9, v12
	v_and_or_b32 v13, v15, s9, v14
	global_store_dwordx2 v[16:17], v[12:13], off sc1
	ds_read_b128 v[16:19], v1 offset:2048
	ds_read_b128 v[20:23], v1 offset:3072
	ds_read_b128 v[24:27], v1 offset:6144
	ds_read_b128 v[28:31], v1 offset:7168
	ds_read_b128 v[32:35], v1 offset:10240
	ds_read_b128 v[36:39], v1 offset:11264
	ds_read_b128 v[40:43], v1 offset:14336
	ds_read_b128 v[44:47], v1 offset:15360
	ds_read_b128 v[48:51], v1 offset:18432
	ds_read_b128 v[52:55], v1 offset:19456
	ds_read_b128 v[56:59], v1 offset:22528
	ds_read_b128 v[60:63], v1 offset:23552
	ds_read_b128 v[64:67], v1 offset:26624
	ds_read_b128 v[68:71], v1 offset:27648
	ds_read_b128 v[72:75], v1 offset:30720
	ds_read_b128 v[76:79], v1 offset:31744
	s_waitcnt lgkmcnt(13)
	v_pk_add_f32 v[18:19], v[18:19], v[26:27]
	v_pk_add_f32 v[16:17], v[16:17], v[24:25]
	s_waitcnt lgkmcnt(11)
	v_pk_add_f32 v[18:19], v[18:19], v[34:35]
	v_pk_add_f32 v[16:17], v[16:17], v[32:33]
	s_waitcnt lgkmcnt(9)
	v_pk_add_f32 v[18:19], v[18:19], v[42:43]
	v_pk_add_f32 v[16:17], v[16:17], v[40:41]
	s_waitcnt lgkmcnt(7)
	v_pk_add_f32 v[18:19], v[18:19], v[50:51]
	v_pk_add_f32 v[16:17], v[16:17], v[48:49]
	s_waitcnt lgkmcnt(5)
	v_pk_add_f32 v[18:19], v[18:19], v[58:59]
	v_pk_add_f32 v[16:17], v[16:17], v[56:57]
	s_waitcnt lgkmcnt(3)
	v_pk_add_f32 v[18:19], v[18:19], v[66:67]
	v_pk_add_f32 v[16:17], v[16:17], v[64:65]
	s_waitcnt lgkmcnt(1)
	v_pk_add_f32 v[18:19], v[18:19], v[74:75]
	v_pk_add_f32 v[16:17], v[16:17], v[72:73]
	v_pk_add_f32 v[20:21], v[20:21], v[28:29]
	s_waitcnt vmcnt(3)
	v_pk_add_f32 v[14:15], v[18:19], v[94:95]
	v_pk_add_f32 v[12:13], v[16:17], v[92:93]
	v_bfe_u32 v18, v14, 16, 1
	v_bfe_u32 v16, v12, 16, 1
	v_bfe_u32 v17, v13, 16, 1
	v_bfe_u32 v19, v15, 16, 1
	v_add3_u32 v12, v12, v16, s8
	v_add3_u32 v14, v14, v18, s8
	v_add3_u32 v13, v13, v17, s8
	v_add3_u32 v15, v15, v19, s8
	v_lshrrev_b32_e32 v12, 16, v12
	v_lshrrev_b32_e32 v14, 16, v14
	v_and_or_b32 v12, v13, s9, v12
	v_and_or_b32 v13, v15, s9, v14
	global_store_dwordx2 v[84:85], v[12:13], off sc1
	v_pk_add_f32 v[18:19], v[22:23], v[30:31]
	v_pk_add_f32 v[20:21], v[20:21], v[36:37]
	v_pk_add_f32 v[18:19], v[18:19], v[38:39]
	v_pk_add_f32 v[20:21], v[20:21], v[44:45]
	v_pk_add_f32 v[18:19], v[18:19], v[46:47]
	v_pk_add_f32 v[20:21], v[20:21], v[52:53]
	v_pk_add_f32 v[18:19], v[18:19], v[54:55]
	v_pk_add_f32 v[20:21], v[20:21], v[60:61]
	v_pk_add_f32 v[18:19], v[18:19], v[62:63]
	v_pk_add_f32 v[20:21], v[20:21], v[68:69]
	v_pk_add_f32 v[18:19], v[18:19], v[70:71]
	s_waitcnt lgkmcnt(0)
	v_pk_add_f32 v[20:21], v[20:21], v[76:77]
	v_pk_add_f32 v[18:19], v[18:19], v[78:79]
	v_add_u32_e32 v16, 48, v80
	v_ashrrev_i32_e32 v17, 31, v16
	s_waitcnt vmcnt(3)
	v_pk_add_f32 v[14:15], v[18:19], v[98:99]
	v_pk_add_f32 v[12:13], v[20:21], v[96:97]
	v_bfe_u32 v20, v14, 16, 1
	v_bfe_u32 v18, v12, 16, 1
	v_bfe_u32 v19, v13, 16, 1
	v_bfe_u32 v21, v15, 16, 1
	v_add3_u32 v12, v12, v18, s8
	v_add3_u32 v14, v14, v20, s8
	v_add3_u32 v13, v13, v19, s8
	v_add3_u32 v15, v15, v21, s8
	v_lshrrev_b32_e32 v12, 16, v12
	v_lshrrev_b32_e32 v14, 16, v14
	v_and_or_b32 v12, v13, s9, v12
	v_and_or_b32 v13, v15, s9, v14
	v_lshl_add_u64 v[14:15], v[16:17], 1, v[8:9]
	global_store_dwordx2 v[14:15], v[12:13], off sc1
	s_branch .LBB0_816
